# baseline (speedup 1.0000x reference)
.LBB2_10:
	s_setprio 0
	v_add_u32_e32 v106, v73, v112
	ds_read_b128 v[74:77], v106
	v_add_u32_e32 v94, s13, v112
	v_add_u32_e32 v78, 0x1f200, v94
	ds_read_b128 v[78:81], v78
	ds_read_b128 v[82:85], v106 offset:64
	s_waitcnt vmcnt(11) lgkmcnt(0)
	v_mfma_f32_16x16x32_bf16 v[86:89], v[74:77], v[24:27], v[78:81]
	s_waitcnt vmcnt(7)
	v_mfma_f32_16x16x32_bf16 v[90:93], v[74:77], v[64:67], v[78:81]
	s_waitcnt vmcnt(3)
	v_mfma_f32_16x16x32_bf16 v[74:77], v[74:77], v[68:71], v[78:81]
	v_mfma_f32_16x16x32_bf16 v[78:81], v[82:85], v[20:23], v[86:89]
	v_mfma_f32_16x16x32_bf16 v[86:89], v[82:85], v[56:59], v[90:93]
	s_waitcnt vmcnt(2)
	v_mfma_f32_16x16x32_bf16 v[74:77], v[82:85], v[60:63], v[74:77]
	ds_read_b128 v[82:85], v106 offset:128
	s_nop 0
	ds_read_b128 v[90:93], v106 offset:192
	s_waitcnt lgkmcnt(1)
	v_mfma_f32_16x16x32_bf16 v[86:89], v[82:85], v[40:43], v[86:89]
	v_mfma_f32_16x16x32_bf16 v[78:81], v[82:85], v[16:19], v[78:81]
	s_waitcnt vmcnt(1)
	v_mfma_f32_16x16x32_bf16 v[74:77], v[82:85], v[44:47], v[74:77]
	s_waitcnt lgkmcnt(0)
	v_mfma_f32_16x16x32_bf16 v[82:85], v[90:93], v[28:31], v[86:89]
	s_nop 2
	ds_read_b128 v[86:89], v106 offset:4352
	v_mfma_f32_16x16x32_bf16 v[78:81], v[90:93], v[12:15], v[78:81]
	s_waitcnt vmcnt(0)
	v_mfma_f32_16x16x32_bf16 v[74:77], v[90:93], v[32:35], v[74:77]
	v_add_u32_e32 v90, 0x1f240, v94
	ds_read_b128 v[90:93], v90
	ds_read_b128 v[94:97], v106 offset:4416
	s_waitcnt lgkmcnt(1)
	v_mfma_f32_16x16x32_bf16 v[98:101], v[86:89], v[24:27], v[90:93]
	v_mfma_f32_16x16x32_bf16 v[102:105], v[86:89], v[64:67], v[90:93]
	v_mfma_f32_16x16x32_bf16 v[86:89], v[86:89], v[68:71], v[90:93]
	s_waitcnt lgkmcnt(0)
	v_mfma_f32_16x16x32_bf16 v[90:93], v[94:97], v[20:23], v[98:101]
	v_mfma_f32_16x16x32_bf16 v[98:101], v[94:97], v[56:59], v[102:105]
	v_mfma_f32_16x16x32_bf16 v[86:89], v[94:97], v[60:63], v[86:89]
	ds_read_b128 v[94:97], v106 offset:4480
	s_nop 1
	ds_read_b128 v[102:105], v106 offset:4544
	s_waitcnt lgkmcnt(1)
	v_mfma_f32_16x16x32_bf16 v[90:93], v[94:97], v[16:19], v[90:93]
	v_mfma_f32_16x16x32_bf16 v[98:101], v[94:97], v[40:43], v[98:101]
	v_mfma_f32_16x16x32_bf16 v[86:89], v[94:97], v[44:47], v[86:89]
	s_waitcnt lgkmcnt(0)
	v_mfma_f32_16x16x32_bf16 v[90:93], v[102:105], v[12:15], v[90:93]
	v_mfma_f32_16x16x32_bf16 v[94:97], v[102:105], v[28:31], v[98:101]
	v_mfma_f32_16x16x32_bf16 v[86:89], v[102:105], v[32:35], v[86:89]
	s_setprio 2
	s_nop 1
	v_exp_f32_e32 v99, v78
	v_exp_f32_e32 v100, v79
	v_exp_f32_e32 v101, v80
	v_exp_f32_e32 v102, v81
	v_exp_f32_e32 v90, v90
	v_exp_f32_e32 v91, v91
	v_exp_f32_e32 v92, v92
	v_exp_f32_e32 v93, v93
	v_exp_f32_e32 v103, v74
	v_exp_f32_e32 v104, v75
	v_exp_f32_e32 v105, v76
	v_exp_f32_e32 v106, v77
	v_exp_f32_e32 v88, v88
	v_exp_f32_e32 v89, v89
	v_add_u32_e32 v98, v72, v112
	v_exp_f32_e32 v82, v82
	v_exp_f32_e32 v83, v83
	v_exp_f32_e32 v84, v84
	v_exp_f32_e32 v85, v85
	v_add_u32_e32 v74, 0x17600, v98
	v_add_u32_e32 v78, 0x1a300, v98
	v_add_f32_e32 v98, 1.0, v99
	v_add_f32_e32 v99, 1.0, v100
	v_add_f32_e32 v100, 1.0, v101
	v_add_f32_e32 v101, 1.0, v102
	v_add_f32_e32 v90, 1.0, v90
	v_add_f32_e32 v91, 1.0, v91
	v_add_f32_e32 v92, 1.0, v92
	v_add_f32_e32 v93, 1.0, v93
	v_exp_f32_e32 v94, v94
	v_exp_f32_e32 v95, v95
	v_exp_f32_e32 v96, v96
	v_exp_f32_e32 v97, v97
	v_exp_f32_e32 v86, v86
	v_exp_f32_e32 v87, v87
	ds_read_b128 v[74:77], v74
	ds_read_b128 v[78:81], v78
	v_add_f32_e32 v102, 1.0, v103
	v_add_f32_e32 v103, 1.0, v104
	v_add_f32_e32 v104, 1.0, v105
	v_add_f32_e32 v105, 1.0, v106
	v_add_f32_e32 v106, 1.0, v88
	v_add_f32_e32 v107, 1.0, v89
	v_mul_f32_e32 v121, v98, v99
	v_mul_f32_e32 v122, v100, v101
	v_mul_f32_e32 v124, v90, v91
	v_mul_f32_e32 v125, v92, v93
	v_rcp_f32_e32 v121, v121
	v_rcp_f32_e32 v122, v122
	v_rcp_f32_e32 v124, v124
	v_rcp_f32_e32 v125, v125
	v_add_f32_e32 v119, 1.0, v82
	v_add_f32_e32 v120, 1.0, v83
	v_add_f32_e32 v126, 1.0, v84
	v_add_f32_e32 v127, 1.0, v85
	v_add_f32_e32 v94, 1.0, v94
	v_add_f32_e32 v95, 1.0, v95
	v_add_f32_e32 v96, 1.0, v96
	v_add_f32_e32 v97, 1.0, v97
	v_mul_f32_e32 v99, v121, v99
	v_mul_f32_e32 v98, v121, v98
	v_mul_f32_e32 v101, v122, v101
	v_mul_f32_e32 v100, v122, v100
	v_mul_f32_e32 v91, v124, v91
	v_mul_f32_e32 v90, v124, v90
	v_mul_f32_e32 v93, v125, v93
	v_mul_f32_e32 v92, v125, v92
	v_cvt_pk_bf16_f32 v82, v99, v98
	v_cvt_pk_bf16_f32 v83, v101, v100
	v_cvt_pk_bf16_f32 v84, v91, v90
	v_cvt_pk_bf16_f32 v85, v93, v92
	v_mul_f32_e32 v121, v119, v120
	v_mul_f32_e32 v122, v126, v127
	v_mul_f32_e32 v124, v94, v95
	v_mul_f32_e32 v125, v96, v97
	v_rcp_f32_e32 v121, v121
	v_rcp_f32_e32 v122, v122
	v_rcp_f32_e32 v124, v124
	v_rcp_f32_e32 v125, v125
	s_waitcnt lgkmcnt(1)
	v_mfma_f32_16x16x32_bf16 v[52:55], v[74:77], v[82:85], v[52:55]
	v_add_f32_e32 v98, 1.0, v86
	v_add_f32_e32 v99, 1.0, v87
	v_mul_f32_e32 v100, v102, v103
	v_mul_f32_e32 v101, v104, v105
	v_mul_f32_e32 v91, v106, v107
	v_mul_f32_e32 v90, v98, v99
	s_waitcnt lgkmcnt(0)
	v_mfma_f32_16x16x32_bf16 v[0:3], v[78:81], v[82:85], v[0:3]
	v_rcp_f32_e32 v100, v100
	v_rcp_f32_e32 v101, v101
	v_rcp_f32_e32 v90, v90
	v_rcp_f32_e32 v91, v91
	v_mul_f32_e32 v120, v121, v120
	v_mul_f32_e32 v119, v121, v119
	v_mul_f32_e32 v127, v122, v127
	v_mul_f32_e32 v126, v122, v126
	v_mul_f32_e32 v95, v124, v95
	v_mul_f32_e32 v94, v124, v94
	v_mul_f32_e32 v97, v125, v97
	v_mul_f32_e32 v96, v125, v96
	v_cvt_pk_bf16_f32 v86, v120, v119
	v_cvt_pk_bf16_f32 v87, v127, v126
	v_cvt_pk_bf16_f32 v88, v95, v94
	v_cvt_pk_bf16_f32 v89, v97, v96
	v_mul_f32_e32 v103, v100, v103
	v_mul_f32_e32 v102, v100, v102
	v_mul_f32_e32 v105, v101, v105
	v_mul_f32_e32 v104, v101, v104
	v_mul_f32_e32 v99, v90, v99
	v_mul_f32_e32 v98, v90, v98
	v_mul_f32_e32 v107, v91, v107
	v_mul_f32_e32 v106, v91, v106
	v_mfma_f32_16x16x32_bf16 v[48:51], v[74:77], v[86:89], v[48:51]
	s_add_i32 s12, s12, -1
	s_addk_i32 s13, 0x80
	v_add_u32_e32 v73, 0x2200, v73
	v_cvt_pk_bf16_f32 v82, v103, v102
	v_cvt_pk_bf16_f32 v83, v105, v104
	v_cvt_pk_bf16_f32 v84, v99, v98
	v_cvt_pk_bf16_f32 v85, v107, v106
	v_mfma_f32_16x16x32_bf16 v[4:7], v[78:81], v[86:89], v[4:7]
	s_cmp_eq_u32 s12, 0
	v_add_u32_e32 v72, 64, v72
	s_nop 0
	v_mfma_f32_16x16x32_bf16 v[36:39], v[74:77], v[82:85], v[36:39]
	v_mfma_f32_16x16x32_bf16 v[8:11], v[78:81], v[82:85], v[8:11]
	s_cbranch_scc0 .LBB2_10
	ds_read_b128 v[72:75], v117
	ds_read_b128 v[76:79], v117 offset:64
	s_waitcnt lgkmcnt(1)
	v_mfma_f32_16x16x32_bf16 v[80:83], v[72:75], v[24:27], 0
	v_mfma_f32_16x16x32_bf16 v[84:87], v[72:75], v[64:67], 0
	v_mfma_f32_16x16x32_bf16 v[72:75], v[72:75], v[68:71], 0
	s_waitcnt lgkmcnt(0)
	v_mfma_f32_16x16x32_bf16 v[88:91], v[76:79], v[20:23], v[80:83]
	s_nop 3
	ds_read_b128 v[80:83], v117 offset:128
	ds_read_b128 v[96:99], v117 offset:192
	v_mfma_f32_16x16x32_bf16 v[84:87], v[76:79], v[56:59], v[84:87]
	v_mfma_f32_16x16x32_bf16 v[100:103], v[76:79], v[60:63], v[72:75]
	s_nop 2
	v_add_u32_e32 v72, 0, v112
	v_add_u32_e32 v92, 0x1f780, v72
	ds_read_b128 v[72:75], v92
	s_waitcnt lgkmcnt(2)
	v_mfma_f32_16x16x32_bf16 v[84:87], v[80:83], v[40:43], v[84:87]
	s_waitcnt lgkmcnt(0)
	v_add_f32_e32 v52, v72, v52
	v_mfma_f32_16x16x32_bf16 v[104:107], v[80:83], v[16:19], v[88:91]
	v_add_f32_e32 v48, v72, v48
	v_exp_f32_e32 v52, v52
	v_exp_f32_e32 v48, v48
	v_mfma_f32_16x16x32_bf16 v[80:83], v[80:83], v[44:47], v[100:103]
	v_add_f32_e32 v36, v72, v36
	v_exp_f32_e32 v36, v36
	v_add_f32_e32 v72, v52, v48
	v_mfma_f32_16x16x32_bf16 v[84:87], v[96:99], v[28:31], v[84:87]
	ds_read_b128 v[88:91], v117 offset:4352
	ds_read_b128 v[76:79], v117 offset:4416
	ds_read_b128 v[92:95], v92 offset:64
	v_add_f32_e32 v72, v72, v36
	v_add_f32_e32 v49, v73, v49
	v_mfma_f32_16x16x32_bf16 v[100:103], v[96:99], v[12:15], v[104:107]
	s_nop 1
	v_mul_f32_e32 v48, v48, v84
	v_exp_f32_e32 v49, v49
	v_add_f32_e32 v37, v73, v37
	v_mfma_f32_16x16x32_bf16 v[80:83], v[96:99], v[32:35], v[80:83]
	v_exp_f32_e32 v37, v37
	s_nop 0
	v_fmac_f32_e32 v48, v52, v100
	v_add_f32_e32 v52, v73, v53
	v_exp_f32_e32 v52, v52
	s_waitcnt lgkmcnt(2)
	v_mfma_f32_16x16x32_bf16 v[24:27], v[88:91], v[24:27], 0
	s_nop 0
	v_fmac_f32_e32 v48, v36, v80
	v_add_f32_dpp v36, v72, v72 quad_perm:[1,0,3,2] row_mask:0xf bank_mask:0xf bound_ctrl:1
	ds_read_b128 v[104:107], v117 offset:4480
	ds_read_b128 v[120:123], v117 offset:4544
	v_add_f32_dpp v36, v36, v36 quad_perm:[2,3,0,1] row_mask:0xf bank_mask:0xf bound_ctrl:1
	v_add_f32_dpp v48, v48, v48 quad_perm:[1,0,3,2] row_mask:0xf bank_mask:0xf bound_ctrl:1
	v_mfma_f32_16x16x32_bf16 v[64:67], v[88:91], v[64:67], 0
	v_add_f32_dpp v36, v36, v36 row_half_mirror row_mask:0xf bank_mask:0xf bound_ctrl:1
	v_add_f32_dpp v48, v48, v48 quad_perm:[2,3,0,1] row_mask:0xf bank_mask:0xf bound_ctrl:1
	v_add_f32_e32 v50, v74, v50
	v_add_f32_dpp v36, v36, v36 row_mirror row_mask:0xf bank_mask:0xf bound_ctrl:1
	v_rcp_f32_e32 v36, v36
	v_add_f32_dpp v48, v48, v48 row_half_mirror row_mask:0xf bank_mask:0xf bound_ctrl:1
	s_waitcnt lgkmcnt(3)
	v_mfma_f32_16x16x32_bf16 v[20:23], v[76:79], v[20:23], v[24:27]
	v_exp_f32_e32 v50, v50
	v_add_f32_dpp v48, v48, v48 row_mirror row_mask:0xf bank_mask:0xf bound_ctrl:1
	v_fma_f32 v36, v36, v48, 0
	v_add_f32_e32 v48, v52, v49
	v_mul_f32_e32 v49, v49, v85
	v_add_f32_e32 v48, v48, v37
	v_fmac_f32_e32 v49, v52, v101
	v_fmac_f32_e32 v49, v37, v81
	v_mfma_f32_16x16x32_bf16 v[68:71], v[88:91], v[68:71], 0
	v_add_f32_dpp v37, v48, v48 quad_perm:[1,0,3,2] row_mask:0xf bank_mask:0xf bound_ctrl:1
	v_add_f32_dpp v24, v49, v49 quad_perm:[1,0,3,2] row_mask:0xf bank_mask:0xf bound_ctrl:1
	v_add_f32_e32 v49, v74, v54
	v_add_f32_dpp v37, v37, v37 quad_perm:[2,3,0,1] row_mask:0xf bank_mask:0xf bound_ctrl:1
	v_add_f32_dpp v48, v24, v24 quad_perm:[2,3,0,1] row_mask:0xf bank_mask:0xf bound_ctrl:1
	v_mfma_f32_16x16x32_bf16 v[24:27], v[76:79], v[56:59], v[64:67]
	v_add_f32_dpp v37, v37, v37 row_half_mirror row_mask:0xf bank_mask:0xf bound_ctrl:1
	v_exp_f32_e32 v49, v49
	v_add_f32_dpp v48, v48, v48 row_half_mirror row_mask:0xf bank_mask:0xf bound_ctrl:1
	v_add_f32_dpp v37, v37, v37 row_mirror row_mask:0xf bank_mask:0xf bound_ctrl:1
	s_waitcnt lgkmcnt(1)
	v_mfma_f32_16x16x32_bf16 v[16:19], v[104:107], v[16:19], v[20:23]
	v_rcp_f32_e32 v37, v37
	v_add_f32_dpp v48, v48, v48 row_mirror row_mask:0xf bank_mask:0xf bound_ctrl:1
	v_add_f32_e32 v0, v92, v0
	v_add_f32_e32 v20, v74, v38
	v_mfma_f32_16x16x32_bf16 v[56:59], v[76:79], v[60:63], v[68:71]
	v_exp_f32_e32 v38, v20
	v_fmac_f32_e32 v36, v37, v48
	v_add_f32_e32 v4, v92, v4
	v_mfma_f32_16x16x32_bf16 v[20:23], v[104:107], v[40:43], v[24:27]
	v_mul_f32_e32 v40, v50, v86
	v_fmac_f32_e32 v40, v49, v102
	v_fmac_f32_e32 v40, v38, v82
	v_add_f32_e32 v24, v49, v50
	v_add_f32_e32 v37, v24, v38
	v_mfma_f32_16x16x32_bf16 v[24:27], v[104:107], v[44:47], v[56:59]
	v_exp_f32_e32 v0, v0
	v_exp_f32_e32 v4, v4
	v_add_f32_e32 v8, v92, v8
	s_waitcnt lgkmcnt(0)
	v_mfma_f32_16x16x32_bf16 v[12:15], v[120:123], v[12:15], v[16:19]
	v_exp_f32_e32 v8, v8
	v_add_f32_e32 v1, v93, v1
	v_add_f32_e32 v5, v93, v5
	v_add_f32_dpp v16, v37, v37 quad_perm:[1,0,3,2] row_mask:0xf bank_mask:0xf bound_ctrl:1
	v_exp_f32_e32 v1, v1
	v_exp_f32_e32 v5, v5
	v_add_f32_dpp v16, v16, v16 quad_perm:[2,3,0,1] row_mask:0xf bank_mask:0xf bound_ctrl:1
	v_add_f32_e32 v2, v94, v2
	v_exp_f32_e32 v2, v2
	v_add_f32_dpp v37, v16, v16 row_half_mirror row_mask:0xf bank_mask:0xf bound_ctrl:1
	v_mfma_f32_16x16x32_bf16 v[16:19], v[120:123], v[28:31], v[20:23]
	s_nop 0
	v_add_f32_dpp v28, v37, v37 row_mirror row_mask:0xf bank_mask:0xf bound_ctrl:1
	s_nop 0
	v_add_f32_dpp v20, v40, v40 quad_perm:[1,0,3,2] row_mask:0xf bank_mask:0xf bound_ctrl:1
	s_nop 1
	v_add_f32_dpp v29, v20, v20 quad_perm:[2,3,0,1] row_mask:0xf bank_mask:0xf bound_ctrl:1
	v_mfma_f32_16x16x32_bf16 v[20:23], v[120:123], v[32:35], v[24:27]
	s_nop 2
	v_add_f32_e32 v26, v75, v55
	v_add_f32_e32 v27, v75, v51
	v_rcp_f32_e32 v25, v28
	v_exp_f32_e32 v26, v26
	v_exp_f32_e32 v27, v27
	v_add_f32_e32 v28, v75, v39
	v_exp_f32_e32 v28, v28
	v_add_f32_dpp v24, v29, v29 row_half_mirror row_mask:0xf bank_mask:0xf bound_ctrl:1
	s_nop 1
	v_add_f32_dpp v24, v24, v24 row_mirror row_mask:0xf bank_mask:0xf bound_ctrl:1
	v_fmac_f32_e32 v36, v25, v24
	v_add_f32_e32 v24, v26, v27
	v_add_f32_e32 v24, v24, v28
	v_mul_f32_e32 v25, v27, v87
	v_fmac_f32_e32 v25, v26, v103
	v_add_f32_dpp v24, v24, v24 quad_perm:[1,0,3,2] row_mask:0xf bank_mask:0xf bound_ctrl:1
	v_fmac_f32_e32 v25, v28, v83
	s_nop 0
	v_add_f32_dpp v24, v24, v24 quad_perm:[2,3,0,1] row_mask:0xf bank_mask:0xf bound_ctrl:1
	v_add_f32_dpp v25, v25, v25 quad_perm:[1,0,3,2] row_mask:0xf bank_mask:0xf bound_ctrl:1
	s_nop 0
	v_add_f32_dpp v24, v24, v24 row_half_mirror row_mask:0xf bank_mask:0xf bound_ctrl:1
	v_add_f32_dpp v25, v25, v25 quad_perm:[2,3,0,1] row_mask:0xf bank_mask:0xf bound_ctrl:1
	s_nop 0
	v_add_f32_dpp v24, v24, v24 row_mirror row_mask:0xf bank_mask:0xf bound_ctrl:1
	v_rcp_f32_e32 v24, v24
	v_add_f32_dpp v25, v25, v25 row_half_mirror row_mask:0xf bank_mask:0xf bound_ctrl:1
	s_nop 1
	v_add_f32_dpp v25, v25, v25 row_mirror row_mask:0xf bank_mask:0xf bound_ctrl:1
	v_fmac_f32_e32 v36, v24, v25
	v_add_f32_e32 v24, v0, v4
	v_add_f32_e32 v24, v24, v8
	v_mul_f32_e32 v4, v4, v16
	v_fmac_f32_e32 v4, v0, v12
	v_add_f32_dpp v0, v24, v24 quad_perm:[1,0,3,2] row_mask:0xf bank_mask:0xf bound_ctrl:1
	v_fmac_f32_e32 v4, v8, v20
	v_add_f32_e32 v8, v93, v9
	v_add_f32_dpp v0, v0, v0 quad_perm:[2,3,0,1] row_mask:0xf bank_mask:0xf bound_ctrl:1
	v_add_f32_dpp v4, v4, v4 quad_perm:[1,0,3,2] row_mask:0xf bank_mask:0xf bound_ctrl:1
	v_exp_f32_e32 v8, v8
	v_add_f32_dpp v0, v0, v0 row_half_mirror row_mask:0xf bank_mask:0xf bound_ctrl:1
	v_add_f32_dpp v4, v4, v4 quad_perm:[2,3,0,1] row_mask:0xf bank_mask:0xf bound_ctrl:1
	s_nop 0
	v_add_f32_dpp v0, v0, v0 row_mirror row_mask:0xf bank_mask:0xf bound_ctrl:1
	v_rcp_f32_e32 v0, v0
	v_add_f32_dpp v4, v4, v4 row_half_mirror row_mask:0xf bank_mask:0xf bound_ctrl:1
	s_nop 1
	v_add_f32_dpp v4, v4, v4 row_mirror row_mask:0xf bank_mask:0xf bound_ctrl:1
	v_fmac_f32_e32 v36, v0, v4
	v_add_f32_e32 v0, v1, v5
	v_add_f32_e32 v0, v0, v8
	v_mul_f32_e32 v4, v5, v17
	v_fmac_f32_e32 v4, v1, v13
	v_add_f32_dpp v0, v0, v0 quad_perm:[1,0,3,2] row_mask:0xf bank_mask:0xf bound_ctrl:1
	v_fmac_f32_e32 v4, v8, v21
	v_add_f32_e32 v5, v94, v10
	v_add_f32_dpp v0, v0, v0 quad_perm:[2,3,0,1] row_mask:0xf bank_mask:0xf bound_ctrl:1
	v_add_f32_dpp v1, v4, v4 quad_perm:[1,0,3,2] row_mask:0xf bank_mask:0xf bound_ctrl:1
	v_add_f32_e32 v4, v94, v6
	v_add_f32_dpp v0, v0, v0 row_half_mirror row_mask:0xf bank_mask:0xf bound_ctrl:1
	v_exp_f32_e32 v4, v4
	v_add_f32_dpp v1, v1, v1 quad_perm:[2,3,0,1] row_mask:0xf bank_mask:0xf bound_ctrl:1
	v_add_f32_dpp v0, v0, v0 row_mirror row_mask:0xf bank_mask:0xf bound_ctrl:1
	v_rcp_f32_e32 v0, v0
	v_exp_f32_e32 v5, v5
	v_add_f32_dpp v1, v1, v1 row_half_mirror row_mask:0xf bank_mask:0xf bound_ctrl:1
	s_nop 1
	v_add_f32_dpp v1, v1, v1 row_mirror row_mask:0xf bank_mask:0xf bound_ctrl:1
	v_fmac_f32_e32 v36, v0, v1
	v_add_f32_e32 v0, v2, v4
	v_add_f32_e32 v0, v0, v5
	v_mul_f32_e32 v1, v4, v18
	v_fmac_f32_e32 v1, v2, v14
	v_add_f32_dpp v0, v0, v0 quad_perm:[1,0,3,2] row_mask:0xf bank_mask:0xf bound_ctrl:1
	v_fmac_f32_e32 v1, v5, v22
	v_add_f32_e32 v2, v95, v3
	v_add_f32_dpp v0, v0, v0 quad_perm:[2,3,0,1] row_mask:0xf bank_mask:0xf bound_ctrl:1
	v_add_f32_e32 v3, v95, v7
	v_add_f32_dpp v1, v1, v1 quad_perm:[1,0,3,2] row_mask:0xf bank_mask:0xf bound_ctrl:1
	v_add_f32_dpp v0, v0, v0 row_half_mirror row_mask:0xf bank_mask:0xf bound_ctrl:1
	v_exp_f32_e32 v2, v2
	v_exp_f32_e32 v3, v3
	v_add_f32_dpp v0, v0, v0 row_mirror row_mask:0xf bank_mask:0xf bound_ctrl:1
	v_rcp_f32_e32 v0, v0
	v_add_f32_e32 v4, v95, v11
	v_add_f32_dpp v1, v1, v1 quad_perm:[2,3,0,1] row_mask:0xf bank_mask:0xf bound_ctrl:1
	v_exp_f32_e32 v4, v4
	s_nop 0
	v_add_f32_dpp v1, v1, v1 row_half_mirror row_mask:0xf bank_mask:0xf bound_ctrl:1
	s_nop 1
	v_add_f32_dpp v1, v1, v1 row_mirror row_mask:0xf bank_mask:0xf bound_ctrl:1
	v_fmac_f32_e32 v36, v0, v1
	v_add_f32_e32 v0, v2, v3
	v_add_f32_e32 v0, v0, v4
	v_mul_f32_e32 v1, v3, v19
	v_fmac_f32_e32 v1, v2, v15
	v_add_f32_dpp v0, v0, v0 quad_perm:[1,0,3,2] row_mask:0xf bank_mask:0xf bound_ctrl:1
	v_fmac_f32_e32 v1, v4, v23
	s_nop 0
	v_add_f32_dpp v0, v0, v0 quad_perm:[2,3,0,1] row_mask:0xf bank_mask:0xf bound_ctrl:1
	v_add_f32_dpp v1, v1, v1 quad_perm:[1,0,3,2] row_mask:0xf bank_mask:0xf bound_ctrl:1
	s_nop 0
	v_add_f32_dpp v0, v0, v0 row_half_mirror row_mask:0xf bank_mask:0xf bound_ctrl:1
	v_add_f32_dpp v1, v1, v1 quad_perm:[2,3,0,1] row_mask:0xf bank_mask:0xf bound_ctrl:1
	s_nop 0
	v_add_f32_dpp v0, v0, v0 row_mirror row_mask:0xf bank_mask:0xf bound_ctrl:1
	v_rcp_f32_e32 v0, v0
	v_add_f32_dpp v1, v1, v1 row_half_mirror row_mask:0xf bank_mask:0xf bound_ctrl:1
	s_nop 1
	v_add_f32_dpp v1, v1, v1 row_mirror row_mask:0xf bank_mask:0xf bound_ctrl:1
	v_fmac_f32_e32 v36, v0, v1
	s_nop 0
	v_readlane_b32 s20, v36, 0
	v_readlane_b32 s23, v36, 16
	v_readlane_b32 s21, v36, 32
	v_readlane_b32 s22, v36, 48
	s_and_saveexec_b64 s[12:13], s[0:1]
	s_cbranch_execz .LBB2_8
	v_lshlrev_b64 v[0:1], 2, v[110:111]
	v_lshl_add_u64 v[2:3], s[4:5], 0, v[0:1]
	global_load_dword v4, v[2:3], off
	v_lshl_add_u64 v[2:3], s[6:7], 0, v[0:1]
	global_load_dword v5, v[2:3], off
	v_mov_b32_e32 v2, s23
	v_add_f32_e32 v2, s20, v2
	v_add_f32_e32 v2, s21, v2
	v_add_f32_e32 v2, s22, v2
	v_add_f32_e32 v6, s14, v2
	v_max_f32_e64 v7, -v6, 0
	v_mul_f32_e32 v2, 0xbfb8aa3b, v6
	v_sub_f32_e64 v8, -v6, v7
	v_exp_f32_e32 v2, v2
	v_mul_f32_e32 v3, 0xbfb8aa3b, v7
	v_mul_f32_e32 v8, 0x3fb8aa3b, v8
	v_exp_f32_e32 v3, v3
	v_exp_f32_e32 v8, v8
	v_add_f32_e32 v2, 1.0, v2
	v_rcp_f32_e32 v9, v2
	v_add_f32_e32 v2, v3, v8
	v_cmp_gt_f32_e32 vcc, s17, v2
	s_and_b64 s[20:21], vcc, exec
	s_cselect_b32 s20, 32, 0
	v_ldexp_f32 v2, v2, s20
	v_log_f32_e32 v10, v2
	v_lshl_add_u64 v[2:3], s[8:9], 0, v[0:1]
	global_store_dword v[2:3], v9, off
	v_cndmask_b32_e32 v8, 0, v118, vcc
	v_mul_f32_e32 v2, 0x3f317217, v10
	v_fma_f32 v2, v10, s18, -v2
	v_fmac_f32_e32 v2, 0x3377d1cf, v10
	v_fmac_f32_e32 v2, 0x3f317217, v10
	v_cmp_lt_f32_e64 vcc, |v10|, s19
	v_lshl_add_u64 v[0:1], s[10:11], 0, v[0:1]
	s_waitcnt vmcnt(2)
	v_fma_f32 v3, -v6, v4, v6
	v_cndmask_b32_e32 v2, v10, v2, vcc
	v_sub_f32_e32 v2, v2, v8
	v_add_f32_e32 v3, v7, v3
	v_add_f32_e32 v2, v2, v3
	s_waitcnt vmcnt(1)
	v_mul_f32_e32 v2, v5, v2
	global_store_dword v[0:1], v2, off
	s_branch .LBB2_8

	.amdhsa_kernel _Z11attn_kernelPKtS0_PKfS2_S2_PfS3_
		.amdhsa_group_segment_fixed_size 0
		.amdhsa_private_segment_fixed_size 0
		.amdhsa_kernarg_size 56
		.amdhsa_user_sgpr_count 2
		.amdhsa_user_sgpr_dispatch_ptr 0
		.amdhsa_user_sgpr_queue_ptr 0
		.amdhsa_user_sgpr_kernarg_segment_ptr 1
		.amdhsa_user_sgpr_dispatch_id 0
		.amdhsa_user_sgpr_kernarg_preload_length 0
		.amdhsa_user_sgpr_kernarg_preload_offset 0
		.amdhsa_user_sgpr_private_segment_size 0
		.amdhsa_uses_dynamic_stack 0
		.amdhsa_enable_private_segment 0
		.amdhsa_system_sgpr_workgroup_id_x 1
		.amdhsa_system_sgpr_workgroup_id_y 0
		.amdhsa_system_sgpr_workgroup_id_z 0
		.amdhsa_system_sgpr_workgroup_info 0
		.amdhsa_system_vgpr_workitem_id 0
		.amdhsa_next_free_vgpr 128
		.amdhsa_next_free_sgpr 24
		.amdhsa_accum_offset 128
		.amdhsa_reserve_vcc 1
		.amdhsa_float_round_mode_32 0
		.amdhsa_float_round_mode_16_64 0
		.amdhsa_float_denorm_mode_32 3
		.amdhsa_float_denorm_mode_16_64 3
		.amdhsa_dx10_clamp 1
		.amdhsa_ieee_mode 1
		.amdhsa_fp16_overflow 0
		.amdhsa_tg_split 0
		.amdhsa_exception_fp_ieee_invalid_op 0
		.amdhsa_exception_fp_denorm_src 0
		.amdhsa_exception_fp_ieee_div_zero 0
		.amdhsa_exception_fp_ieee_overflow 0
		.amdhsa_exception_fp_ieee_underflow 0
		.amdhsa_exception_fp_ieee_inexact 0
		.amdhsa_exception_int_div_zero 0
	.end_amdhsa_kernel

amdhsa.kernels:
  - .agpr_count:     0
    .args:
      - .actual_access:  read_only
        .address_space:  global
        .offset:         0
        .size:           8
        .value_kind:     global_buffer
      - .actual_access:  read_only
        .address_space:  global
        .offset:         8
        .size:           8
        .value_kind:     global_buffer
      - .actual_access:  read_only
        .address_space:  global
        .offset:         16
        .size:           8
        .value_kind:     global_buffer
      - .actual_access:  read_only
        .address_space:  global
        .offset:         24
        .size:           8
        .value_kind:     global_buffer
      - .actual_access:  read_only
        .address_space:  global
        .offset:         32
        .size:           8
        .value_kind:     global_buffer
      - .actual_access:  read_only
        .address_space:  global
        .offset:         40
        .size:           8
        .value_kind:     global_buffer
      - .actual_access:  read_only
        .address_space:  global
        .offset:         48
        .size:           8
        .value_kind:     global_buffer
      - .actual_access:  read_only
        .address_space:  global
        .offset:         56
        .size:           8
        .value_kind:     global_buffer
      - .actual_access:  read_only
        .address_space:  global
        .offset:         64
        .size:           8
        .value_kind:     global_buffer
      - .actual_access:  read_only
        .address_space:  global
        .offset:         72
        .size:           8
        .value_kind:     global_buffer
      - .actual_access:  read_only
        .address_space:  global
        .offset:         80
        .size:           8
        .value_kind:     global_buffer
      - .actual_access:  read_only
        .address_space:  global
        .offset:         88
        .size:           8
        .value_kind:     global_buffer
      - .actual_access:  read_only
        .address_space:  global
        .offset:         96
        .size:           8
        .value_kind:     global_buffer
      - .actual_access:  read_only
        .address_space:  global
        .offset:         104
        .size:           8
        .value_kind:     global_buffer
      - .actual_access:  read_only
        .address_space:  global
        .offset:         112
        .size:           8
        .value_kind:     global_buffer
      - .actual_access:  read_only
        .address_space:  global
        .offset:         120
        .size:           8
        .value_kind:     global_buffer
      - .actual_access:  write_only
        .address_space:  global
        .offset:         128
        .size:           8
        .value_kind:     global_buffer
      - .actual_access:  write_only
        .address_space:  global
        .offset:         136
        .size:           8
        .value_kind:     global_buffer
      - .actual_access:  write_only
        .address_space:  global
        .offset:         144
        .size:           8
        .value_kind:     global_buffer
    .group_segment_fixed_size: 0
    .kernarg_segment_align: 8
    .kernarg_segment_size: 152
    .language:       OpenCL C
    .language_version:
      - 2
      - 0
    .max_flat_workgroup_size: 256
    .name:           _Z11prep_kernelPKfS0_S0_S0_S0_S0_S0_S0_S0_S0_S0_S0_S0_S0_S0_S0_PtS1_S1_
    .private_segment_fixed_size: 0
    .sgpr_count:     30
    .sgpr_spill_count: 0
    .symbol:         _Z11prep_kernelPKfS0_S0_S0_S0_S0_S0_S0_S0_S0_S0_S0_S0_S0_S0_S0_PtS1_S1_.kd
    .uniform_work_group_size: 1
    .uses_dynamic_stack: false
    .vgpr_count:     8
    .vgpr_spill_count: 0
    .wavefront_size: 64
  - .agpr_count:     0
    .args:
      - .actual_access:  read_only
        .address_space:  global
        .offset:         0
        .size:           8
        .value_kind:     global_buffer
      - .actual_access:  read_only
        .address_space:  global
        .offset:         8
        .size:           8
        .value_kind:     global_buffer
      - .actual_access:  read_only
        .address_space:  global
        .offset:         16
        .size:           8
        .value_kind:     global_buffer
      - .actual_access:  read_only
        .address_space:  global
        .offset:         24
        .size:           8
        .value_kind:     global_buffer
      - .actual_access:  read_only
        .address_space:  global
        .offset:         32
        .size:           8
        .value_kind:     global_buffer
      - .actual_access:  read_only
        .address_space:  global
        .offset:         40
        .size:           8
        .value_kind:     global_buffer
      - .actual_access:  read_only
        .address_space:  global
        .offset:         48
        .size:           8
        .value_kind:     global_buffer
      - .actual_access:  read_only
        .address_space:  global
        .offset:         56
        .size:           8
        .value_kind:     global_buffer
      - .actual_access:  write_only
        .address_space:  global
        .offset:         64
        .size:           8
        .value_kind:     global_buffer
      - .actual_access:  write_only
        .address_space:  global
        .offset:         72
        .size:           8
        .value_kind:     global_buffer
      - .actual_access:  write_only
        .address_space:  global
        .offset:         80
        .size:           8
        .value_kind:     global_buffer
    .group_segment_fixed_size: 0
    .kernarg_segment_align: 8
    .kernarg_segment_size: 88
    .language:       OpenCL C
    .language_version:
      - 2
      - 0
    .max_flat_workgroup_size: 512
    .name:           _Z10rnn_kernelPKfS0_S0_S0_S0_S0_PKtS2_PfPtS3_
    .private_segment_fixed_size: 0
    .sgpr_count:     82
    .sgpr_spill_count: 0
    .symbol:         _Z10rnn_kernelPKfS0_S0_S0_S0_S0_PKtS2_PfPtS3_.kd
    .uniform_work_group_size: 1
    .uses_dynamic_stack: false
    .vgpr_count:     256
    .vgpr_spill_count: 0
    .wavefront_size: 64
  - .agpr_count:     0
    .args:
      - .actual_access:  read_only
        .address_space:  global
        .offset:         0
        .size:           8
        .value_kind:     global_buffer
      - .actual_access:  read_only
        .address_space:  global
        .offset:         8
        .size:           8
        .value_kind:     global_buffer
      - .actual_access:  read_only
        .address_space:  global
        .offset:         16
        .size:           8
        .value_kind:     global_buffer
      - .actual_access:  read_only
        .address_space:  global
        .offset:         24
        .size:           8
        .value_kind:     global_buffer
      - .actual_access:  read_only
        .address_space:  global
        .offset:         32
        .size:           8
        .value_kind:     global_buffer
      - .actual_access:  write_only
        .address_space:  global
        .offset:         40
        .size:           8
        .value_kind:     global_buffer
      - .actual_access:  write_only
        .address_space:  global
        .offset:         48
        .size:           8
        .value_kind:     global_buffer
    .group_segment_fixed_size: 0
    .kernarg_segment_align: 8
    .kernarg_segment_size: 56
    .language:       OpenCL C
    .language_version:
      - 2
      - 0
    .max_flat_workgroup_size: 1024
    .name:           _Z11attn_kernelPKtS0_PKfS2_S2_PfS3_
    .private_segment_fixed_size: 0
    .sgpr_count:     30
    .sgpr_spill_count: 0
    .symbol:         _Z11attn_kernelPKtS0_PKfS2_S2_PfS3_.kd
    .uniform_work_group_size: 1
    .uses_dynamic_stack: false
    .vgpr_count:     128
    .vgpr_spill_count: 0
    .wavefront_size: 64
  - .agpr_count:     0
    .args:
      - .actual_access:  read_only
        .address_space:  global
        .offset:         0
        .size:           8
        .value_kind:     global_buffer
      - .actual_access:  read_only
        .address_space:  global
        .offset:         8
        .size:           8
        .value_kind:     global_buffer
      - .actual_access:  read_only
        .address_space:  global
        .offset:         16
        .size:           8
        .value_kind:     global_buffer
      - .actual_access:  write_only
        .address_space:  global
        .offset:         24
        .size:           8
        .value_kind:     global_buffer
    .group_segment_fixed_size: 192
    .kernarg_segment_align: 8
    .kernarg_segment_size: 32
    .language:       OpenCL C
    .language_version:
      - 2
      - 0
    .max_flat_workgroup_size: 1024
    .name:           _Z11loss_kernelPKfS0_S0_Pf
    .private_segment_fixed_size: 0
    .sgpr_count:     14
    .sgpr_spill_count: 0
    .symbol:         _Z11loss_kernelPKfS0_S0_Pf.kd
    .uniform_work_group_size: 1
    .uses_dynamic_stack: false
    .vgpr_count:     46
    .vgpr_spill_count: 0
    .wavefront_size: 64
